# speedup vs baseline: 1.0501x; 1.0349x over previous
.LBB0_29:
	s_or_b64 exec, exec, s[36:37]
	s_mul_i32 s36, s2, 0x104
	v_add_u32_e32 v48, s36, v0
	v_ashrrev_i32_e32 v49, 31, v48
	s_movk_i32 s0, 0xff
	s_waitcnt lgkmcnt(0)
	v_lshl_add_u64 v[48:49], v[48:49], 2, s[18:19]
	v_cmp_eq_u32_e64 s[0:1], s0, v0
	ds_write_b32 v19, v46 offset:33024
	global_store_dword v[48:49], v46, off sc1
	s_and_b64 exec, exec, s[0:1]
	s_cbranch_execz .LBB0_31
	s_ashr_i32 s37, s36, 31
	s_lshl_b64 s[0:1], s[36:37], 2
	s_add_u32 s0, s18, s0
	s_addc_u32 s1, s19, s1
	v_mov_b32_e32 v45, 0
	v_add_u32_e32 v44, v46, v44
	global_store_dword v45, v44, s[0:1] offset:1024 sc1

.LBB0_40:
	s_or_b64 exec, exec, s[0:1]
	s_waitcnt lgkmcnt(0)
	s_barrier
	ds_read_b128 v[2:5], v1
	s_add_u32 s0, s30, s28
	s_addc_u32 s1, s31, s29
	s_waitcnt lgkmcnt(0)
	global_store_dwordx4 v1, v[2:5], s[0:1] sc1
	s_and_saveexec_b64 s[4:5], vcc
	s_cbranch_execz .LBB0_42
	ds_read_b128 v[2:5], v1 offset:16384
	s_waitcnt lgkmcnt(0)
	global_store_dwordx4 v18, v[2:5], s[0:1] sc1
.LBB0_42:
	s_or_b64 exec, exec, s[4:5]
	s_nop 0
	v_lshl_or_b32 v2, s2, 10, v0
	s_movk_i32 s0, 0x4000
	v_cmp_gt_i32_e32 vcc, s0, v2
	v_ashrrev_i32_e32 v3, 31, v2
	s_and_saveexec_b64 s[0:1], vcc
	s_cbranch_execz .LBB0_44
	v_lshrrev_b32_e32 v1, 4, v2
	v_lshrrev_b32_e32 v4, 5, v0
	v_and_b32_e32 v6, 3, v0
	v_and_b32_e32 v1, 0x60, v1
	v_and_b32_e32 v5, 12, v4
	v_and_or_b32 v6, v19, 16, v6
	v_or3_b32 v1, v6, v5, v1
	v_lshlrev_b32_e32 v5, 3, v0
	s_lshl_b32 s3, s2, 4
	v_and_b32_e32 v0, 16, v0
	s_and_b32 s2, s2, -4
	s_and_b32 s3, s3, 32
	v_add_u32_e32 v0, s2, v0
	v_and_or_b32 v5, v5, 64, s3
	v_lshlrev_b32_e32 v1, 7, v1
	v_and_or_b32 v0, v4, 3, v0
	v_add3_u32 v0, v0, v5, v1
	v_ashrrev_i32_e32 v1, 31, v0
	v_lshl_add_u64 v[0:1], v[0:1], 2, s[24:25]
	global_load_dword v0, v[0:1], off
	s_waitcnt vmcnt(0)
	v_cvt_f16_f32_e32 v4, v0
	v_lshl_add_u64 v[0:1], v[2:3], 1, s[26:27]
	global_store_short v[0:1], v4, off sc1
.LBB0_44:
	s_or_b64 exec, exec, s[0:1]
	s_movk_i32 s0, 0x2000
	v_cmp_gt_i32_e32 vcc, s0, v2
	s_and_saveexec_b64 s[0:1], vcc
	s_cbranch_execz .LBB0_46
	v_lshl_add_u64 v[0:1], v[2:3], 2, s[22:23]
	v_mov_b32_e32 v2, 0
	global_store_dword v[0:1], v2, off sc1

.LBB1_71:
	s_or_b64 exec, exec, s[6:7]
	s_and_saveexec_b64 s[6:7], s[0:1]
	s_cbranch_execz .LBB1_73
	v_mov_b32_e32 v73, 0x10000
	v_lshl_or_b32 v73, v0, 2, v73
	ds_read_b32 v73, v73
	v_ashrrev_i32_e32 v75, 31, v74
	v_lshlrev_b64 v[74:75], 2, v[74:75]
	s_waitcnt lgkmcnt(0)
	v_cvt_f32_i32_e32 v76, v73
	v_cmp_gt_i32_e32 vcc, 1, v73
	v_mul_f32_e32 v77, 0x4b800000, v76
	s_nop 0
	v_cndmask_b32_e32 v76, v76, v77, vcc
	v_rsq_f32_e32 v120, v76
	v_lshl_add_u64 v[76:77], s[64:65], 0, v[74:75]
	global_store_dword v[76:77], v73, off sc1
	v_lshl_add_u64 v[74:75], s[66:67], 0, v[74:75]
	v_mul_f32_e32 v73, 0x45800000, v120
	v_cndmask_b32_e32 v73, v120, v73, vcc
	global_store_dword v[74:75], v73, off sc1
.LBB1_73:
	s_or_b64 exec, exec, s[6:7]
	s_add_i32 s1, s55, s3
	s_add_i32 s0, s33, s54
	v_cmp_eq_u32_e64 s[6:7], 0, v0
	s_and_saveexec_b64 s[60:61], s[6:7]
	s_cbranch_execz .LBB1_75
	s_lshl_b32 s64, s2, 1
	s_ashr_i32 s65, s64, 31
	s_lshl_b64 s[64:65], s[64:65], 2
	s_add_u32 s58, s58, s64
	s_addc_u32 s59, s59, s65
	v_mov_b32_e32 v73, 0
	v_mov_b64_e32 v[74:75], s[0:1]
	global_store_dwordx2 v73, v[74:75], s[58:59] sc1
.LBB1_75:
	s_or_b64 exec, exec, s[60:61]
	s_waitcnt lgkmcnt(0)
	s_barrier
	s_cmpk_lt_i32 s1, 0x2001
	s_cselect_b64 s[58:59], -1, 0
	s_cmpk_gt_i32 s1, 0x2000
	s_cselect_b64 s[60:61], -1, 0
	s_and_saveexec_b64 s[64:65], s[42:43]
	s_cbranch_execz .LBB1_80
	v_and_b32_e32 v73, 0x7fc, v119
	v_or_b32_e32 v73, 0x10800, v73
	v_mov_b32_e32 v74, 1
	ds_add_rtn_u32 v73, v73, v74
	s_mov_b64 s[42:43], -1
	s_and_b64 vcc, exec, s[60:61]
	s_cbranch_vccz .LBB1_78
	s_waitcnt lgkmcnt(0)
	v_add_u32_e32 v74, s0, v73
	v_ashrrev_i32_e32 v75, 31, v74
	v_lshl_add_u64 v[74:75], v[74:75], 2, s[56:57]
	global_store_dword v[74:75], v117, off sc1
	s_mov_b64 s[42:43], 0

.LBB1_80:
	s_or_b64 exec, exec, s[64:65]
	s_waitcnt lgkmcnt(0)
	v_cndmask_b32_e64 v73, 0, 1, s[60:61]
	v_cmp_ne_u32_e64 s[42:43], 1, v73
	s_and_saveexec_b64 s[64:65], s[50:51]
	s_cbranch_execz .LBB1_85
	v_and_b32_e32 v73, 0x7fc, v118
	v_or_b32_e32 v73, 0x10800, v73
	v_mov_b32_e32 v74, 1
	ds_add_rtn_u32 v73, v73, v74
	s_and_b64 vcc, exec, s[42:43]
	s_mov_b64 s[50:51], -1
	s_cbranch_vccnz .LBB1_83
	s_waitcnt lgkmcnt(0)
	v_add_u32_e32 v74, s0, v73
	v_ashrrev_i32_e32 v75, 31, v74
	v_lshl_add_u64 v[74:75], v[74:75], 2, s[56:57]
	s_mov_b64 s[50:51], 0
	global_store_dword v[74:75], v115, off sc1

.LBB1_85:
	s_or_b64 exec, exec, s[64:65]
	s_and_saveexec_b64 s[50:51], s[48:49]
	s_cbranch_execz .LBB1_90
	s_waitcnt lgkmcnt(0)
	v_and_b32_e32 v73, 0x7fc, v116
	v_or_b32_e32 v73, 0x10800, v73
	v_mov_b32_e32 v74, 1
	ds_add_rtn_u32 v73, v73, v74
	s_and_b64 vcc, exec, s[42:43]
	s_mov_b64 s[48:49], -1
	s_cbranch_vccnz .LBB1_88
	s_waitcnt lgkmcnt(0)
	v_add_u32_e32 v74, s0, v73
	v_ashrrev_i32_e32 v75, 31, v74
	v_lshl_add_u64 v[74:75], v[74:75], 2, s[56:57]
	s_mov_b64 s[48:49], 0
	global_store_dword v[74:75], v113, off sc1

.LBB1_90:
	s_or_b64 exec, exec, s[50:51]
	s_and_saveexec_b64 s[48:49], s[46:47]
	s_cbranch_execz .LBB1_95
	s_waitcnt lgkmcnt(0)
	v_and_b32_e32 v73, 0x7fc, v114
	v_or_b32_e32 v73, 0x10800, v73
	v_mov_b32_e32 v74, 1
	ds_add_rtn_u32 v73, v73, v74
	s_and_b64 vcc, exec, s[42:43]
	s_mov_b64 s[46:47], -1
	s_cbranch_vccnz .LBB1_93
	s_waitcnt lgkmcnt(0)
	v_add_u32_e32 v74, s0, v73
	v_ashrrev_i32_e32 v75, 31, v74
	v_lshl_add_u64 v[74:75], v[74:75], 2, s[56:57]
	s_mov_b64 s[46:47], 0
	global_store_dword v[74:75], v111, off sc1

.LBB1_95:
	s_or_b64 exec, exec, s[48:49]
	s_and_saveexec_b64 s[46:47], s[44:45]
	s_cbranch_execz .LBB1_100
	s_waitcnt lgkmcnt(0)
	v_and_b32_e32 v73, 0x7fc, v112
	v_or_b32_e32 v73, 0x10800, v73
	v_mov_b32_e32 v74, 1
	ds_add_rtn_u32 v73, v73, v74
	s_and_b64 vcc, exec, s[42:43]
	s_mov_b64 s[44:45], -1
	s_cbranch_vccnz .LBB1_98
	s_waitcnt lgkmcnt(0)
	v_add_u32_e32 v74, s0, v73
	v_ashrrev_i32_e32 v75, 31, v74
	v_lshl_add_u64 v[74:75], v[74:75], 2, s[56:57]
	s_mov_b64 s[44:45], 0
	global_store_dword v[74:75], v109, off sc1

.LBB1_100:
	s_or_b64 exec, exec, s[46:47]
	s_and_saveexec_b64 s[44:45], s[40:41]
	s_cbranch_execz .LBB1_105
	s_waitcnt lgkmcnt(0)
	v_and_b32_e32 v73, 0x7fc, v110
	v_or_b32_e32 v73, 0x10800, v73
	v_mov_b32_e32 v74, 1
	ds_add_rtn_u32 v73, v73, v74
	s_and_b64 vcc, exec, s[42:43]
	s_mov_b64 s[40:41], -1
	s_cbranch_vccnz .LBB1_103
	s_waitcnt lgkmcnt(0)
	v_add_u32_e32 v74, s0, v73
	v_ashrrev_i32_e32 v75, 31, v74
	v_lshl_add_u64 v[74:75], v[74:75], 2, s[56:57]
	s_mov_b64 s[40:41], 0
	global_store_dword v[74:75], v107, off sc1

.LBB1_105:
	s_or_b64 exec, exec, s[44:45]
	s_and_saveexec_b64 s[40:41], s[38:39]
	s_cbranch_execz .LBB1_110
	s_waitcnt lgkmcnt(0)
	v_and_b32_e32 v73, 0x7fc, v108
	v_or_b32_e32 v73, 0x10800, v73
	v_mov_b32_e32 v74, 1
	ds_add_rtn_u32 v73, v73, v74
	s_and_b64 vcc, exec, s[42:43]
	s_mov_b64 s[38:39], -1
	s_cbranch_vccnz .LBB1_108
	s_waitcnt lgkmcnt(0)
	v_add_u32_e32 v74, s0, v73
	v_ashrrev_i32_e32 v75, 31, v74
	v_lshl_add_u64 v[74:75], v[74:75], 2, s[56:57]
	s_mov_b64 s[38:39], 0
	global_store_dword v[74:75], v105, off sc1

.LBB1_110:
	s_or_b64 exec, exec, s[40:41]
	s_and_saveexec_b64 s[38:39], s[36:37]
	s_cbranch_execz .LBB1_115
	s_waitcnt lgkmcnt(0)
	v_and_b32_e32 v73, 0x7fc, v106
	v_or_b32_e32 v73, 0x10800, v73
	v_mov_b32_e32 v74, 1
	ds_add_rtn_u32 v73, v73, v74
	s_and_b64 vcc, exec, s[42:43]
	s_mov_b64 s[36:37], -1
	s_cbranch_vccnz .LBB1_113
	s_waitcnt lgkmcnt(0)
	v_add_u32_e32 v74, s0, v73
	v_ashrrev_i32_e32 v75, 31, v74
	v_lshl_add_u64 v[74:75], v[74:75], 2, s[56:57]
	s_mov_b64 s[36:37], 0
	global_store_dword v[74:75], v103, off sc1

.LBB1_115:
	s_or_b64 exec, exec, s[38:39]
	s_and_saveexec_b64 s[36:37], s[34:35]
	s_cbranch_execz .LBB1_120
	s_waitcnt lgkmcnt(0)
	v_and_b32_e32 v73, 0x7fc, v104
	v_or_b32_e32 v73, 0x10800, v73
	v_mov_b32_e32 v74, 1
	ds_add_rtn_u32 v73, v73, v74
	s_and_b64 vcc, exec, s[42:43]
	s_mov_b64 s[34:35], -1
	s_cbranch_vccnz .LBB1_118
	s_waitcnt lgkmcnt(0)
	v_add_u32_e32 v74, s0, v73
	v_ashrrev_i32_e32 v75, 31, v74
	v_lshl_add_u64 v[74:75], v[74:75], 2, s[56:57]
	s_mov_b64 s[34:35], 0
	global_store_dword v[74:75], v101, off sc1

.LBB1_120:
	s_or_b64 exec, exec, s[36:37]
	s_and_saveexec_b64 s[34:35], s[30:31]
	s_cbranch_execz .LBB1_125
	s_waitcnt lgkmcnt(0)
	v_and_b32_e32 v73, 0x7fc, v102
	v_or_b32_e32 v73, 0x10800, v73
	v_mov_b32_e32 v74, 1
	ds_add_rtn_u32 v73, v73, v74
	s_and_b64 vcc, exec, s[42:43]
	s_mov_b64 s[30:31], -1
	s_cbranch_vccnz .LBB1_123
	s_waitcnt lgkmcnt(0)
	v_add_u32_e32 v74, s0, v73
	v_ashrrev_i32_e32 v75, 31, v74
	v_lshl_add_u64 v[74:75], v[74:75], 2, s[56:57]
	s_mov_b64 s[30:31], 0
	global_store_dword v[74:75], v99, off sc1

.LBB1_125:
	s_or_b64 exec, exec, s[34:35]
	s_and_saveexec_b64 s[30:31], s[28:29]
	s_cbranch_execz .LBB1_130
	s_waitcnt lgkmcnt(0)
	v_and_b32_e32 v73, 0x7fc, v100
	v_or_b32_e32 v73, 0x10800, v73
	v_mov_b32_e32 v74, 1
	ds_add_rtn_u32 v73, v73, v74
	s_and_b64 vcc, exec, s[42:43]
	s_mov_b64 s[28:29], -1
	s_cbranch_vccnz .LBB1_128
	s_waitcnt lgkmcnt(0)
	v_add_u32_e32 v74, s0, v73
	v_ashrrev_i32_e32 v75, 31, v74
	v_lshl_add_u64 v[74:75], v[74:75], 2, s[56:57]
	s_mov_b64 s[28:29], 0
	global_store_dword v[74:75], v97, off sc1

.LBB1_130:
	s_or_b64 exec, exec, s[30:31]
	s_and_saveexec_b64 s[28:29], s[26:27]
	s_cbranch_execz .LBB1_135
	s_waitcnt lgkmcnt(0)
	v_and_b32_e32 v73, 0x7fc, v98
	v_or_b32_e32 v73, 0x10800, v73
	v_mov_b32_e32 v74, 1
	ds_add_rtn_u32 v73, v73, v74
	s_and_b64 vcc, exec, s[42:43]
	s_mov_b64 s[26:27], -1
	s_cbranch_vccnz .LBB1_133
	s_waitcnt lgkmcnt(0)
	v_add_u32_e32 v74, s0, v73
	v_ashrrev_i32_e32 v75, 31, v74
	v_lshl_add_u64 v[74:75], v[74:75], 2, s[56:57]
	s_mov_b64 s[26:27], 0
	global_store_dword v[74:75], v95, off sc1

.LBB1_135:
	s_or_b64 exec, exec, s[28:29]
	s_and_saveexec_b64 s[26:27], s[24:25]
	s_cbranch_execz .LBB1_140
	s_waitcnt lgkmcnt(0)
	v_and_b32_e32 v73, 0x7fc, v96
	v_or_b32_e32 v73, 0x10800, v73
	v_mov_b32_e32 v74, 1
	ds_add_rtn_u32 v73, v73, v74
	s_and_b64 vcc, exec, s[42:43]
	s_mov_b64 s[24:25], -1
	s_cbranch_vccnz .LBB1_138
	s_waitcnt lgkmcnt(0)
	v_add_u32_e32 v74, s0, v73
	v_ashrrev_i32_e32 v75, 31, v74
	v_lshl_add_u64 v[74:75], v[74:75], 2, s[56:57]
	s_mov_b64 s[24:25], 0
	global_store_dword v[74:75], v93, off sc1

.LBB1_140:
	s_or_b64 exec, exec, s[26:27]
	s_and_saveexec_b64 s[24:25], s[22:23]
	s_cbranch_execz .LBB1_145
	s_waitcnt lgkmcnt(0)
	v_and_b32_e32 v73, 0x7fc, v94
	v_or_b32_e32 v73, 0x10800, v73
	v_mov_b32_e32 v74, 1
	ds_add_rtn_u32 v73, v73, v74
	s_and_b64 vcc, exec, s[42:43]
	s_mov_b64 s[22:23], -1
	s_cbranch_vccnz .LBB1_143
	s_waitcnt lgkmcnt(0)
	v_add_u32_e32 v74, s0, v73
	v_ashrrev_i32_e32 v75, 31, v74
	v_lshl_add_u64 v[74:75], v[74:75], 2, s[56:57]
	s_mov_b64 s[22:23], 0
	global_store_dword v[74:75], v91, off sc1

.LBB1_145:
	s_or_b64 exec, exec, s[24:25]
	s_and_saveexec_b64 s[22:23], s[20:21]
	s_cbranch_execz .LBB1_150
	s_waitcnt lgkmcnt(0)
	v_and_b32_e32 v73, 0x7fc, v92
	v_or_b32_e32 v73, 0x10800, v73
	v_mov_b32_e32 v74, 1
	ds_add_rtn_u32 v73, v73, v74
	s_and_b64 vcc, exec, s[42:43]
	s_mov_b64 s[20:21], -1
	s_cbranch_vccnz .LBB1_148
	s_waitcnt lgkmcnt(0)
	v_add_u32_e32 v74, s0, v73
	v_ashrrev_i32_e32 v75, 31, v74
	v_lshl_add_u64 v[74:75], v[74:75], 2, s[56:57]
	s_mov_b64 s[20:21], 0
	global_store_dword v[74:75], v89, off sc1

.LBB1_150:
	s_or_b64 exec, exec, s[22:23]
	s_and_saveexec_b64 s[20:21], s[18:19]
	s_cbranch_execz .LBB1_155
	s_waitcnt lgkmcnt(0)
	v_and_b32_e32 v73, 0x7fc, v90
	v_or_b32_e32 v73, 0x10800, v73
	v_mov_b32_e32 v74, 1
	ds_add_rtn_u32 v73, v73, v74
	s_and_b64 vcc, exec, s[42:43]
	s_mov_b64 s[18:19], -1
	s_cbranch_vccnz .LBB1_153
	s_waitcnt lgkmcnt(0)
	v_add_u32_e32 v74, s0, v73
	v_ashrrev_i32_e32 v75, 31, v74
	v_lshl_add_u64 v[74:75], v[74:75], 2, s[56:57]
	s_mov_b64 s[18:19], 0
	global_store_dword v[74:75], v87, off sc1

.LBB1_155:
	s_or_b64 exec, exec, s[20:21]
	s_and_saveexec_b64 s[18:19], s[16:17]
	s_cbranch_execz .LBB1_160
	s_waitcnt lgkmcnt(0)
	v_and_b32_e32 v73, 0x7fc, v88
	v_or_b32_e32 v73, 0x10800, v73
	v_mov_b32_e32 v74, 1
	ds_add_rtn_u32 v73, v73, v74
	s_and_b64 vcc, exec, s[42:43]
	s_mov_b64 s[16:17], -1
	s_cbranch_vccnz .LBB1_158
	s_waitcnt lgkmcnt(0)
	v_add_u32_e32 v74, s0, v73
	v_ashrrev_i32_e32 v75, 31, v74
	v_lshl_add_u64 v[74:75], v[74:75], 2, s[56:57]
	s_mov_b64 s[16:17], 0
	global_store_dword v[74:75], v86, off sc1

.LBB1_163:
	s_waitcnt lgkmcnt(0)
	v_add_u32_e32 v76, v84, v74
	v_ashrrev_i32_e32 v77, 31, v76
	v_lshl_add_u64 v[76:77], v[76:77], 2, s[70:71]
	global_load_dword v75, v[76:77], off
	s_mov_b64 s[18:19], -1
	s_and_b64 vcc, exec, s[60:61]
	s_waitcnt vmcnt(0)
	v_lshrrev_b32_e32 v76, 6, v75
	v_and_b32_e32 v76, 0x7fc, v76
	v_or_b32_e32 v76, 0x10800, v76
	ds_add_rtn_u32 v76, v76, v73
	s_cbranch_vccz .LBB1_165
	s_waitcnt lgkmcnt(0)
	v_add_u32_e32 v86, s0, v76
	v_ashrrev_i32_e32 v87, 31, v86
	v_lshl_add_u64 v[86:87], v[86:87], 2, s[56:57]
	global_store_dword v[86:87], v75, off sc1
	s_mov_b64 s[18:19], 0

.LBB1_170:
	s_waitcnt lgkmcnt(0)
	v_add_u32_e32 v76, v70, v74
	v_ashrrev_i32_e32 v77, 31, v76
	v_lshl_add_u64 v[76:77], v[76:77], 2, s[70:71]
	global_load_dword v75, v[76:77], off
	s_and_b64 vcc, exec, s[42:43]
	s_mov_b64 s[16:17], -1
	s_waitcnt vmcnt(0)
	v_lshrrev_b32_e32 v76, 6, v75
	v_and_b32_e32 v76, 0x7fc, v76
	v_or_b32_e32 v76, 0x10800, v76
	ds_add_rtn_u32 v76, v76, v73
	s_cbranch_vccnz .LBB1_172
	s_waitcnt lgkmcnt(0)
	v_add_u32_e32 v86, s0, v76
	v_ashrrev_i32_e32 v87, 31, v86
	v_lshl_add_u64 v[86:87], v[86:87], 2, s[56:57]
	s_mov_b64 s[16:17], 0
	global_store_dword v[86:87], v75, off sc1

.LBB1_177:
	s_waitcnt lgkmcnt(0)
	v_add_u32_e32 v74, v68, v71
	v_ashrrev_i32_e32 v75, 31, v74
	v_lshl_add_u64 v[74:75], v[74:75], 2, s[70:71]
	s_waitcnt lgkmcnt(0)
	global_load_dword v73, v[74:75], off
	s_and_b64 vcc, exec, s[42:43]
	s_mov_b64 s[14:15], -1
	s_waitcnt vmcnt(0)
	v_lshrrev_b32_e32 v74, 6, v73
	v_and_b32_e32 v74, 0x7fc, v74
	v_or_b32_e32 v74, 0x10800, v74
	ds_add_rtn_u32 v74, v74, v70
	s_cbranch_vccnz .LBB1_179
	s_waitcnt lgkmcnt(0)
	v_add_u32_e32 v76, s0, v74
	v_ashrrev_i32_e32 v77, 31, v76
	v_lshl_add_u64 v[76:77], v[76:77], 2, s[56:57]
	s_mov_b64 s[14:15], 0
	global_store_dword v[76:77], v73, off sc1

.LBB1_184:
	global_load_dword v71, v[68:69], off
	s_and_b64 vcc, exec, s[42:43]
	s_mov_b64 s[12:13], -1
	s_waitcnt vmcnt(0) lgkmcnt(0)
	v_lshrrev_b32_e32 v72, 6, v71
	v_and_b32_e32 v72, 0x7fc, v72
	v_or_b32_e32 v72, 0x10800, v72
	ds_add_rtn_u32 v72, v72, v70
	s_cbranch_vccnz .LBB1_186
	s_waitcnt lgkmcnt(0)
	v_add_u32_e32 v74, s0, v72
	v_ashrrev_i32_e32 v75, 31, v74
	v_lshl_add_u64 v[74:75], v[74:75], 2, s[56:57]
	s_mov_b64 s[12:13], 0
	global_store_dword v[74:75], v71, off sc1

.LBB1_193:
	v_add_u32_e32 v1, 0xffff8000, v85
	v_add_u32_e32 v87, 0xffffa000, v85
	v_add_u32_e32 v86, 0xffff9000, v85
	v_add_u32_e32 v93, 0xffffb000, v85
	v_add_u32_e32 v95, 0xffffc000, v85
	v_add_u32_e32 v99, 0xffffd000, v85
	v_add_u32_e32 v101, 0xffffe000, v85
	v_add_u32_e32 v105, 0xfffff000, v85
	ds_read2st64_b32 v[96:97], v85 offset1:16
	ds_read2st64_b32 v[102:103], v85 offset0:32 offset1:48
	ds_read2st64_b32 v[108:109], v85 offset0:64 offset1:80
	ds_read2st64_b32 v[114:115], v85 offset0:96 offset1:112
	ds_read_b32 v1, v1
	ds_read_b32 v120, v86
	ds_read_b32 v87, v87
	ds_read_b32 v121, v93
	ds_read_b32 v122, v95
	ds_read_b32 v123, v99
	ds_read_b32 v124, v101
	ds_read_b32 v125, v105
	s_waitcnt lgkmcnt(12)
	v_add_u32_e32 v72, s0, v68
	v_add_u32_e32 v84, -8, v84
	v_add_u32_e32 v70, s0, v69
	v_add_u32_e32 v76, s20, v68
	v_add_u32_e32 v74, s21, v69
	v_add_u32_e32 v88, s22, v68
	v_add_u32_e32 v90, s23, v69
	v_add_u32_e32 v92, s24, v68
	v_add_u32_e32 v94, s25, v69
	v_add_u32_e32 v98, s26, v68
	v_add_u32_e32 v100, s27, v69
	v_add_u32_e32 v104, s28, v68
	v_add_u32_e32 v106, s29, v69
	v_add_u32_e32 v110, s30, v68
	v_add_u32_e32 v112, s31, v69
	v_add_u32_e32 v116, s33, v68
	v_add_u32_e32 v118, s34, v69
	s_add_i32 s3, s3, 16
	v_ashrrev_i32_e32 v73, 31, v72
	v_cmp_eq_u32_e32 vcc, 0, v84
	v_add_u32_e32 v69, 0x4000, v69
	v_add_u32_e32 v68, 0x4000, v68
	v_add_u32_e32 v85, 0x10000, v85
	v_ashrrev_i32_e32 v71, 31, v70
	v_ashrrev_i32_e32 v75, 31, v74
	v_ashrrev_i32_e32 v77, 31, v76
	v_ashrrev_i32_e32 v91, 31, v90
	v_ashrrev_i32_e32 v89, 31, v88
	v_ashrrev_i32_e32 v95, 31, v94
	v_ashrrev_i32_e32 v93, 31, v92
	v_ashrrev_i32_e32 v101, 31, v100
	v_ashrrev_i32_e32 v99, 31, v98
	v_ashrrev_i32_e32 v107, 31, v106
	v_ashrrev_i32_e32 v105, 31, v104
	v_ashrrev_i32_e32 v113, 31, v112
	v_ashrrev_i32_e32 v111, 31, v110
	v_ashrrev_i32_e32 v119, 31, v118
	v_ashrrev_i32_e32 v117, 31, v116
	v_mov_b32_e32 v86, s3
	v_lshl_add_u64 v[72:73], v[72:73], 2, s[56:57]
	s_or_b64 s[18:19], vcc, s[18:19]
	v_lshl_add_u64 v[70:71], v[70:71], 2, s[56:57]
	v_lshl_add_u64 v[76:77], v[76:77], 2, s[56:57]
	v_lshl_add_u64 v[74:75], v[74:75], 2, s[56:57]
	v_lshl_add_u64 v[88:89], v[88:89], 2, s[56:57]
	v_lshl_add_u64 v[90:91], v[90:91], 2, s[56:57]
	v_lshl_add_u64 v[92:93], v[92:93], 2, s[56:57]
	v_lshl_add_u64 v[94:95], v[94:95], 2, s[56:57]
	v_lshl_add_u64 v[98:99], v[98:99], 2, s[56:57]
	v_lshl_add_u64 v[100:101], v[100:101], 2, s[56:57]
	v_lshl_add_u64 v[104:105], v[104:105], 2, s[56:57]
	v_lshl_add_u64 v[106:107], v[106:107], 2, s[56:57]
	v_lshl_add_u64 v[110:111], v[110:111], 2, s[56:57]
	v_lshl_add_u64 v[112:113], v[112:113], 2, s[56:57]
	v_lshl_add_u64 v[116:117], v[116:117], 2, s[56:57]
	v_lshl_add_u64 v[118:119], v[118:119], 2, s[56:57]
	s_waitcnt lgkmcnt(7)
	global_store_dword v[72:73], v1, off sc1
	s_waitcnt lgkmcnt(6)
	global_store_dword v[70:71], v120, off sc1
	s_waitcnt lgkmcnt(5)
	global_store_dword v[76:77], v87, off sc1
	s_waitcnt lgkmcnt(4)
	global_store_dword v[74:75], v121, off sc1
	s_waitcnt lgkmcnt(3)
	global_store_dword v[88:89], v122, off sc1
	s_waitcnt lgkmcnt(2)
	global_store_dword v[90:91], v123, off sc1
	s_waitcnt lgkmcnt(1)
	global_store_dword v[92:93], v124, off sc1
	s_waitcnt lgkmcnt(0)
	global_store_dword v[94:95], v125, off sc1
	global_store_dword v[98:99], v96, off sc1
	global_store_dword v[100:101], v97, off sc1
	global_store_dword v[104:105], v102, off sc1
	global_store_dword v[106:107], v103, off sc1
	global_store_dword v[110:111], v108, off sc1
	global_store_dword v[112:113], v109, off sc1
	global_store_dword v[116:117], v114, off sc1
	global_store_dword v[118:119], v115, off sc1
	s_andn2_b64 exec, exec, s[18:19]
	s_cbranch_execnz .LBB1_193
	s_or_b64 exec, exec, s[18:19]

.LBB1_197:
	s_waitcnt lgkmcnt(0)
	ds_read2st64_b32 v[72:73], v70 offset1:16
	v_add_u32_e32 v74, s0, v68
	v_add_u32_e32 v1, -1, v1
	v_add_u32_e32 v76, s0, v69
	v_ashrrev_i32_e32 v75, 31, v74
	v_cmp_eq_u32_e32 vcc, 0, v1
	v_add_u32_e32 v69, 0x800, v69
	v_add_u32_e32 v68, 0x800, v68
	v_add_u32_e32 v70, 0x2000, v70
	v_ashrrev_i32_e32 v77, 31, v76
	v_lshl_add_u64 v[74:75], v[74:75], 2, s[56:57]
	s_or_b64 s[18:19], vcc, s[18:19]
	v_lshl_add_u64 v[76:77], v[76:77], 2, s[56:57]
	s_waitcnt lgkmcnt(0)
	global_store_dword v[74:75], v72, off sc1
	global_store_dword v[76:77], v73, off sc1
	s_andn2_b64 exec, exec, s[18:19]
	s_cbranch_execnz .LBB1_197

.LBB1_202:
	ds_read_b32 v70, v1
	v_add_u32_e32 v0, 0x400, v0
	v_cmp_le_i32_e32 vcc, s1, v0
	v_add_u32_e32 v1, 0x1000, v1
	s_or_b64 s[10:11], vcc, s[10:11]
	s_waitcnt lgkmcnt(0)
	global_store_dword v[68:69], v70, off sc1
	v_lshl_add_u64 v[68:69], v[68:69], 0, s[12:13]
	s_andn2_b64 exec, exec, s[10:11]
	s_cbranch_execnz .LBB1_202

.LBB1_210:
	s_or_b64 exec, exec, s[8:9]
	s_mul_hi_i32 s55, s2, 0x187
	v_lshlrev_b32_e32 v52, 3, v67
	s_and_saveexec_b64 s[0:1], s[52:53]
	s_cbranch_execz .LBB1_212
	s_waitcnt lgkmcnt(0)
	v_cvt_f16_f32_e32 v63, v72
	v_mov_b32_e32 v67, 0
	v_lshl_add_u64 v[64:65], s[54:55], 0, v[66:67]
	v_cvt_pk_f16_f32 v66, v68, v69
	v_cvt_pk_f16_f32 v46, v46, v47
	v_cvt_pk_f16_f32 v47, v58, v59
	v_cvt_f16_f32_e32 v58, v76
	v_cvt_pk_f16_f32 v48, v48, v49
	v_cvt_f16_f32_e32 v49, v75
	v_pack_b32_f16 v80, v63, v46
	v_alignbit_b32 v81, v66, v46, 16
	v_cvt_f16_f32_e32 v46, v61
	v_cvt_pk_f16_f32 v4, v4, v5
	v_cvt_f16_f32_e32 v5, v77
	v_cvt_pk_f16_f32 v8, v8, v9
	v_cvt_pk_f16_f32 v9, v50, v51
	v_alignbit_b32 v82, v47, v66, 16
	v_alignbit_b32 v83, v58, v47, 16
	v_alignbit_b32 v47, v48, v8, 16
	v_alignbit_b32 v48, v9, v48, 16
	v_alignbit_b32 v49, v49, v9, 16
	v_cvt_pk_f16_f32 v9, v44, v45
	v_pack_b32_f16 v46, v46, v8
	v_cvt_f16_f32_e32 v8, v73
	v_alignbit_b32 v44, v4, v9, 16
	v_alignbit_b32 v45, v5, v4, 16
	v_cvt_f16_f32_e32 v4, v74
	v_cvt_f16_f32_e32 v5, v62
	v_lshlrev_b64 v[64:65], 8, v[64:65]
	v_lshl_add_u64 v[64:65], s[68:69], 0, v[64:65]
	v_lshlrev_b32_e32 v66, 1, v52
	v_cvt_pk_f16_f32 v43, v42, v43
	v_cvt_pk_f16_f32 v2, v2, v3
	v_cvt_pk_f16_f32 v1, v0, v1
	v_cvt_pk_f16_f32 v3, v6, v7
	v_lshl_add_u64 v[58:59], v[64:65], 0, v[66:67]
	v_pack_b32_f16 v42, v8, v43
	v_alignbit_b32 v43, v9, v43, 16
	v_pack_b32_f16 v0, v4, v1
	v_alignbit_b32 v1, v2, v1, 16
	v_alignbit_b32 v2, v3, v2, 16
	v_alignbit_b32 v3, v5, v3, 16
	global_store_dwordx4 v[58:59], v[80:83], off sc1
	global_store_dwordx4 v[58:59], v[46:49], off offset:64 sc1
	global_store_dwordx4 v[58:59], v[42:45], off offset:128 sc1
	global_store_dwordx4 v[58:59], v[0:3], off offset:192 sc1

.LBB1_220:
	s_or_b64 exec, exec, s[0:1]
	s_and_b64 exec, exec, s[4:5]
	s_cbranch_execz .LBB1_222
	v_cvt_f16_f32_e32 v3, v35
	v_cvt_pk_f16_f32 v29, v28, v29
	v_cvt_pk_f16_f32 v21, v20, v21
	v_cvt_pk_f16_f32 v13, v12, v13
	v_pack_b32_f16 v28, v3, v29
	v_cvt_f16_f32_e32 v3, v26
	s_waitcnt lgkmcnt(0)
	v_mov_b32_e32 v33, 0
	v_cvt_pk_f16_f32 v24, v24, v25
	v_cvt_f16_f32_e32 v25, v27
	v_pack_b32_f16 v20, v3, v21
	v_cvt_f16_f32_e32 v3, v18
	v_cvt_pk_f16_f32 v16, v16, v17
	v_cvt_f16_f32_e32 v17, v19
	v_cvt_pk_f16_f32 v8, v8, v9
	v_cvt_f16_f32_e32 v9, v11
	v_pack_b32_f16 v12, v3, v13
	v_cvt_f16_f32_e32 v3, v10
	v_cvt_pk_f16_f32 v6, v6, v7
	v_cvt_f16_f32_e32 v7, v2
	v_lshl_add_u64 v[36:37], s[54:55], 0, v[32:33]
	v_lshlrev_b64 v[36:37], 8, v[36:37]
	v_lshl_add_u64 v[36:37], s[68:69], 0, v[36:37]
	v_cvt_pk_f16_f32 v30, v30, v31
	v_lshlrev_b32_e32 v32, 1, v52
	v_cvt_pk_f16_f32 v22, v22, v23
	v_cvt_pk_f16_f32 v14, v14, v15
	v_cvt_pk_f16_f32 v4, v4, v5
	v_cvt_pk_f16_f32 v5, v0, v1
	v_alignbit_b32 v29, v30, v29, 16
	v_alignbit_b32 v30, v24, v30, 16
	v_alignbit_b32 v31, v25, v24, 16
	v_lshl_add_u64 v[24:25], v[36:37], 0, v[32:33]
	v_alignbit_b32 v21, v22, v21, 16
	v_alignbit_b32 v22, v16, v22, 16
	v_alignbit_b32 v23, v17, v16, 16
	v_alignbit_b32 v13, v14, v13, 16
	v_alignbit_b32 v14, v8, v14, 16
	v_alignbit_b32 v15, v9, v8, 16
	v_pack_b32_f16 v0, v3, v4
	v_alignbit_b32 v1, v6, v4, 16
	v_alignbit_b32 v2, v5, v6, 16
	v_alignbit_b32 v3, v7, v5, 16
	global_store_dwordx4 v[24:25], v[28:31], off sc1
	global_store_dwordx4 v[24:25], v[20:23], off offset:64 sc1
	global_store_dwordx4 v[24:25], v[12:15], off offset:128 sc1
	global_store_dwordx4 v[24:25], v[0:3], off offset:192 sc1
.LBB1_222:
	s_or_b64 exec, exec, s[8:9]
	s_waitcnt lgkmcnt(0)
	s_barrier
	s_and_saveexec_b64 s[0:1], s[6:7]
	s_cbranch_execz .LBB1_224
	v_mov_b32_e32 v0, 0x1102c
	ds_read_b32 v0, v0
	s_lshl_b64 s[0:1], s[2:3], 2
	s_add_u32 s0, s62, s0
	s_addc_u32 s1, s63, s1
	v_mov_b32_e32 v1, 0
	s_waitcnt lgkmcnt(0)
	global_store_dword v1, v0, s[0:1] sc1

.LBB2_15:
	v_lshrrev_b32_e32 v43, 3, v0
	s_waitcnt vmcnt(0)
	v_add_u32_e32 v2, s14, v43
	s_add_i32 s16, s16, -1
	v_add_u32_e32 v3, 0x80, v2
	v_min_i32_e32 v4, s16, v3
	v_ashrrev_i32_e32 v5, 31, v4
	v_lshlrev_b64 v[6:7], 2, v[4:5]
	v_lshl_add_u64 v[4:5], s[4:5], 0, v[6:7]
	v_lshl_add_u64 v[6:7], s[18:19], 0, v[6:7]
	v_add_u32_e32 v3, 0x100, v2
	global_load_dword v4, v[4:5], off
	v_mov_b32_e32 v38, 0
	global_load_dword v5, v[6:7], off
	v_min_i32_e32 v6, s16, v3
	v_ashrrev_i32_e32 v7, 31, v6
	v_lshlrev_b64 v[6:7], 2, v[6:7]
	v_lshl_add_u64 v[8:9], s[4:5], 0, v[6:7]
	v_lshl_add_u64 v[6:7], s[18:19], 0, v[6:7]
	v_add_u32_e32 v3, 0x180, v2
	global_load_dword v49, v[6:7], off
	v_min_i32_e32 v6, s16, v3
	v_ashrrev_i32_e32 v7, 31, v6
	v_lshlrev_b64 v[6:7], 2, v[6:7]
	global_load_dword v48, v[8:9], off
	v_lshl_add_u64 v[8:9], s[4:5], 0, v[6:7]
	v_lshl_add_u64 v[6:7], s[18:19], 0, v[6:7]
	global_load_dword v44, v[8:9], off
	global_load_dword v46, v[6:7], off
	v_lshlrev_b32_e32 v3, 3, v0
	v_and_b32_e32 v42, 56, v3
	v_add_u32_e32 v45, 0xfa800000, v19
	v_lshlrev_b32_e32 v47, 2, v42
	v_cmp_gt_i32_e32 vcc, s15, v43
	v_mov_b32_e32 v39, 0
	v_mov_b32_e32 v34, 0
	v_mov_b32_e32 v35, v38
	v_mov_b32_e32 v30, v38
	v_mov_b32_e32 v31, v38
	v_mov_b32_e32 v24, v38
	v_mov_b32_e32 v25, v38
	v_mov_b32_e32 v20, v38
	v_mov_b32_e32 v21, v38
	v_mov_b32_e32 v16, v38
	v_mov_b32_e32 v17, v38
	v_mov_b32_e32 v14, v38
	v_mov_b32_e32 v15, v38
	v_mov_b32_e32 v10, v38
	v_mov_b32_e32 v11, v38
	v_mov_b32_e32 v40, 0
	v_mov_b32_e32 v41, 0
	v_mov_b32_e32 v36, 0
	v_mov_b32_e32 v37, v38
	v_mov_b32_e32 v32, v38
	v_mov_b32_e32 v33, v38
	v_mov_b32_e32 v26, v38
	v_mov_b32_e32 v27, v38
	v_mov_b32_e32 v28, v38
	v_mov_b32_e32 v29, v38
	v_mov_b32_e32 v22, v38
	v_mov_b32_e32 v23, v38
	v_mov_b32_e32 v18, v38
	v_mov_b32_e32 v19, v38
	v_mov_b32_e32 v12, v38
	v_mov_b32_e32 v13, v38
	s_waitcnt lgkmcnt(0)
	s_barrier
	s_and_saveexec_b64 s[0:1], vcc
	s_cbranch_execz .LBB2_17
	v_min_i32_e32 v6, s16, v2
	v_ashrrev_i32_e32 v7, 31, v6
	v_lshlrev_b64 v[6:7], 2, v[6:7]
	v_lshl_add_u64 v[8:9], s[4:5], 0, v[6:7]
	v_lshl_add_u64 v[6:7], s[18:19], 0, v[6:7]
	global_load_dword v23, v[6:7], off
	global_load_dword v22, v[8:9], off
	s_movk_i32 s5, 0x140
	v_mad_u32_u24 v10, v43, s5, v47
	ds_read_b128 v[6:9], v10
	ds_read_b128 v[10:13], v10 offset:16
	v_ashrrev_i32_e32 v3, 31, v2
	v_lshlrev_b64 v[2:3], 8, v[2:3]
	v_lshlrev_b32_e32 v14, 1, v42
	v_mov_b32_e32 v15, 0
	v_lshl_add_u64 v[2:3], s[8:9], 0, v[2:3]
	v_lshl_add_u64 v[2:3], v[2:3], 0, v[14:15]
	s_waitcnt lgkmcnt(1)
	v_cvt_f32_i32_sdwa v15, sext(v7) dst_sel:DWORD dst_unused:UNUSED_PAD src0_sel:WORD_0
	v_cvt_f32_i32_sdwa v14, sext(v6) dst_sel:DWORD dst_unused:UNUSED_PAD src0_sel:WORD_0
	v_cvt_f32_i32_sdwa v17, sext(v9) dst_sel:DWORD dst_unused:UNUSED_PAD src0_sel:WORD_0
	v_cvt_f32_i32_sdwa v16, sext(v8) dst_sel:DWORD dst_unused:UNUSED_PAD src0_sel:WORD_0
	s_waitcnt lgkmcnt(0)
	v_cvt_f32_i32_sdwa v19, sext(v11) dst_sel:DWORD dst_unused:UNUSED_PAD src0_sel:WORD_0
	v_cvt_f32_i32_sdwa v18, sext(v10) dst_sel:DWORD dst_unused:UNUSED_PAD src0_sel:WORD_0
	s_mov_b32 s4, 0xb4c00000
	v_cvt_f32_i32_sdwa v21, sext(v13) dst_sel:DWORD dst_unused:UNUSED_PAD src0_sel:WORD_0
	v_cvt_f32_i32_sdwa v20, sext(v12) dst_sel:DWORD dst_unused:UNUSED_PAD src0_sel:WORD_0
	s_waitcnt vmcnt(1)
	v_mul_lo_u32 v26, v23, s4
	s_waitcnt vmcnt(0)
	v_mul_f32_e32 v28, v22, v45
	v_add_u32_e32 v29, v6, v26
	v_add_u32_e32 v34, v7, v26
	v_add_u32_e32 v35, v8, v26
	v_add_u32_e32 v38, v9, v26
	v_add_u32_e32 v39, v10, v26
	v_add_u32_e32 v52, v11, v26
	v_add_u32_e32 v53, v12, v26
	v_add_u32_e32 v54, v13, v26
	v_pk_mul_f32 v[22:23], v[28:29], v[14:15] op_sel_hi:[0,1]
	v_pk_mul_f32 v[24:25], v[28:29], v[16:17] op_sel_hi:[0,1]
	v_pk_mul_f32 v[30:31], v[28:29], v[18:19] op_sel_hi:[0,1]
	v_pk_fma_f32 v[32:33], v[28:29], v[18:19], 0 op_sel_hi:[0,1,0]
	v_pk_fma_f32 v[36:37], v[28:29], v[16:17], 0 op_sel_hi:[0,1,0]
	v_pk_fma_f32 v[40:41], v[28:29], v[14:15], 0 op_sel_hi:[0,1,0]
	v_sub_u32_sdwa v14, v34, sext(v7) dst_sel:DWORD dst_unused:UNUSED_PAD src0_sel:DWORD src1_sel:WORD_0
	v_sub_u32_sdwa v15, v29, sext(v6) dst_sel:DWORD dst_unused:UNUSED_PAD src0_sel:DWORD src1_sel:WORD_0
	v_sub_u32_sdwa v16, v38, sext(v9) dst_sel:DWORD dst_unused:UNUSED_PAD src0_sel:DWORD src1_sel:WORD_0
	v_sub_u32_sdwa v17, v35, sext(v8) dst_sel:DWORD dst_unused:UNUSED_PAD src0_sel:DWORD src1_sel:WORD_0
	v_sub_u32_sdwa v18, v52, sext(v11) dst_sel:DWORD dst_unused:UNUSED_PAD src0_sel:DWORD src1_sel:WORD_0
	v_sub_u32_sdwa v19, v39, sext(v10) dst_sel:DWORD dst_unused:UNUSED_PAD src0_sel:DWORD src1_sel:WORD_0
	v_sub_u32_sdwa v13, v54, sext(v13) dst_sel:DWORD dst_unused:UNUSED_PAD src0_sel:DWORD src1_sel:WORD_0
	v_sub_u32_sdwa v12, v53, sext(v12) dst_sel:DWORD dst_unused:UNUSED_PAD src0_sel:DWORD src1_sel:WORD_0
	v_cvt_f32_i32_sdwa v11, sext(v14) dst_sel:DWORD dst_unused:UNUSED_PAD src0_sel:WORD_1
	v_cvt_f32_i32_sdwa v10, sext(v15) dst_sel:DWORD dst_unused:UNUSED_PAD src0_sel:WORD_1
	v_cvt_f32_i32_sdwa v15, sext(v16) dst_sel:DWORD dst_unused:UNUSED_PAD src0_sel:WORD_1
	v_cvt_f32_i32_sdwa v14, sext(v17) dst_sel:DWORD dst_unused:UNUSED_PAD src0_sel:WORD_1
	v_cvt_f32_i32_sdwa v17, sext(v18) dst_sel:DWORD dst_unused:UNUSED_PAD src0_sel:WORD_1
	v_cvt_f32_i32_sdwa v16, sext(v19) dst_sel:DWORD dst_unused:UNUSED_PAD src0_sel:WORD_1
	v_cvt_f32_i32_sdwa v13, sext(v13) dst_sel:DWORD dst_unused:UNUSED_PAD src0_sel:WORD_1
	v_cvt_f32_i32_sdwa v12, sext(v12) dst_sel:DWORD dst_unused:UNUSED_PAD src0_sel:WORD_1
	v_pk_mul_f32 v[50:51], v[28:29], v[20:21] op_sel_hi:[0,1]
	v_pk_fma_f32 v[26:27], v[28:29], v[20:21], 0 op_sel_hi:[0,1,0]
	v_pk_mul_f32 v[20:21], v[28:29], v[10:11] op_sel_hi:[0,1]
	v_pk_mul_f32 v[54:55], v[28:29], v[14:15] op_sel_hi:[0,1]
	v_pk_mul_f32 v[56:57], v[28:29], v[16:17] op_sel_hi:[0,1]
	v_pk_mul_f32 v[58:59], v[28:29], v[12:13] op_sel_hi:[0,1]
	v_cvt_pk_f16_f32 v6, v22, v23
	v_cvt_pk_f16_f32 v7, v24, v25
	v_cvt_pk_f16_f32 v8, v30, v31
	v_cvt_pk_f16_f32 v9, v50, v51
	v_pk_mul_f32 v[38:39], v[22:23], v[22:23]
	v_pk_mul_f32 v[34:35], v[24:25], v[24:25]
	v_pk_mul_f32 v[30:31], v[30:31], v[30:31]
	v_pk_mul_f32 v[24:25], v[50:51], v[50:51]
	v_pk_fma_f32 v[12:13], v[28:29], v[12:13], 0 op_sel_hi:[0,1,0]
	v_pk_fma_f32 v[18:19], v[28:29], v[16:17], 0 op_sel_hi:[0,1,0]
	v_pk_fma_f32 v[22:23], v[28:29], v[14:15], 0 op_sel_hi:[0,1,0]
	v_pk_fma_f32 v[28:29], v[28:29], v[10:11], 0 op_sel_hi:[0,1,0]
	v_cvt_pk_f16_f32 v50, v20, v21
	v_pk_mul_f32 v[20:21], v[20:21], v[20:21]
	v_pk_mul_f32 v[16:17], v[54:55], v[54:55]
	v_pk_mul_f32 v[14:15], v[56:57], v[56:57]
	v_pk_mul_f32 v[10:11], v[58:59], v[58:59]
	v_cvt_pk_f16_f32 v51, v54, v55
	v_cvt_pk_f16_f32 v52, v56, v57
	v_cvt_pk_f16_f32 v53, v58, v59
	global_store_dwordx4 v[2:3], v[6:9], off sc1
	global_store_dwordx4 v[2:3], v[50:53], off offset:128 sc1
.LBB2_17:
	s_or_b64 exec, exec, s[0:1]
	s_and_saveexec_b64 s[0:1], vcc
	s_xor_b64 s[0:1], exec, s[0:1]
	s_cbranch_execz .LBB2_29
	v_or_b32_e32 v50, 0x80, v43
	v_cmp_gt_u32_e32 vcc, s15, v50
	s_and_saveexec_b64 s[4:5], vcc
	s_cbranch_execz .LBB2_20
	s_movk_i32 s6, 0x140
	v_mad_u32_u24 v2, v50, s6, v47
	ds_read_b128 v[6:9], v2
	ds_read_b128 v[52:55], v2 offset:16
	s_mov_b32 s6, 0xb4c00000
	s_waitcnt vmcnt(4)
	v_mul_lo_u32 v51, v5, s6
	v_mul_f32_e32 v58, v4, v45
	s_waitcnt lgkmcnt(1)
	v_add_u32_e32 v2, v6, v51
	v_add_u32_e32 v3, v7, v51
	v_sub_u32_sdwa v3, v3, sext(v7) dst_sel:DWORD dst_unused:UNUSED_PAD src0_sel:DWORD src1_sel:WORD_0
	v_sub_u32_sdwa v2, v2, sext(v6) dst_sel:DWORD dst_unused:UNUSED_PAD src0_sel:DWORD src1_sel:WORD_0
	v_cvt_f32_i32_sdwa v57, sext(v3) dst_sel:DWORD dst_unused:UNUSED_PAD src0_sel:WORD_1
	v_cvt_f32_i32_sdwa v56, sext(v2) dst_sel:DWORD dst_unused:UNUSED_PAD src0_sel:WORD_1
	v_cvt_f32_i32_sdwa v62, sext(v6) dst_sel:DWORD dst_unused:UNUSED_PAD src0_sel:WORD_0
	v_add_u32_e32 v3, v8, v51
	v_add_u32_e32 v6, v9, v51
	v_cvt_f32_i32_sdwa v63, sext(v7) dst_sel:DWORD dst_unused:UNUSED_PAD src0_sel:WORD_0
	v_sub_u32_sdwa v6, v6, sext(v9) dst_sel:DWORD dst_unused:UNUSED_PAD src0_sel:DWORD src1_sel:WORD_0
	v_sub_u32_sdwa v3, v3, sext(v8) dst_sel:DWORD dst_unused:UNUSED_PAD src0_sel:DWORD src1_sel:WORD_0
	v_pk_mul_f32 v[4:5], v[58:59], v[56:57] op_sel_hi:[0,1]
	v_pk_fma_f32 v[28:29], v[58:59], v[56:57], v[28:29] op_sel_hi:[0,1,1]
	v_cvt_f32_i32_sdwa v57, sext(v6) dst_sel:DWORD dst_unused:UNUSED_PAD src0_sel:WORD_1
	v_cvt_f32_i32_sdwa v56, sext(v3) dst_sel:DWORD dst_unused:UNUSED_PAD src0_sel:WORD_1
	v_cvt_pk_f16_f32 v2, v4, v5
	v_pk_fma_f32 v[20:21], v[4:5], v[4:5], v[20:21]
	v_pk_mul_f32 v[4:5], v[58:59], v[62:63] op_sel_hi:[0,1]
	v_cvt_pk_f16_f32 v6, v4, v5
	v_pk_fma_f32 v[38:39], v[4:5], v[4:5], v[38:39]
	v_pk_mul_f32 v[4:5], v[58:59], v[56:57] op_sel_hi:[0,1]
	v_pk_fma_f32 v[22:23], v[58:59], v[56:57], v[22:23] op_sel_hi:[0,1,1]
	s_waitcnt lgkmcnt(0)
	v_add_u32_e32 v7, v52, v51
	v_add_u32_e32 v56, v53, v51
	v_sub_u32_sdwa v56, v56, sext(v53) dst_sel:DWORD dst_unused:UNUSED_PAD src0_sel:DWORD src1_sel:WORD_0
	v_sub_u32_sdwa v7, v7, sext(v52) dst_sel:DWORD dst_unused:UNUSED_PAD src0_sel:DWORD src1_sel:WORD_0
	v_cvt_f32_i32_sdwa v9, sext(v9) dst_sel:DWORD dst_unused:UNUSED_PAD src0_sel:WORD_0
	v_cvt_f32_i32_sdwa v8, sext(v8) dst_sel:DWORD dst_unused:UNUSED_PAD src0_sel:WORD_0
	v_cvt_f32_i32_sdwa v57, sext(v56) dst_sel:DWORD dst_unused:UNUSED_PAD src0_sel:WORD_1
	v_cvt_f32_i32_sdwa v56, sext(v7) dst_sel:DWORD dst_unused:UNUSED_PAD src0_sel:WORD_1
	v_cvt_pk_f16_f32 v3, v4, v5
	v_pk_fma_f32 v[16:17], v[4:5], v[4:5], v[16:17]
	v_pk_mul_f32 v[4:5], v[58:59], v[8:9] op_sel_hi:[0,1]
	v_pk_fma_f32 v[36:37], v[58:59], v[8:9], v[36:37] op_sel_hi:[0,1,1]
	v_pk_mul_f32 v[8:9], v[58:59], v[56:57] op_sel_hi:[0,1]
	v_cvt_pk_f16_f32 v7, v4, v5
	v_pk_fma_f32 v[34:35], v[4:5], v[4:5], v[34:35]
	v_cvt_pk_f16_f32 v4, v8, v9
	v_pk_fma_f32 v[14:15], v[8:9], v[8:9], v[14:15]
	v_add_u32_e32 v5, v54, v51
	v_add_u32_e32 v8, v55, v51
	v_sub_u32_sdwa v8, v8, sext(v55) dst_sel:DWORD dst_unused:UNUSED_PAD src0_sel:DWORD src1_sel:WORD_0
	v_sub_u32_sdwa v5, v5, sext(v54) dst_sel:DWORD dst_unused:UNUSED_PAD src0_sel:DWORD src1_sel:WORD_0
	v_pk_fma_f32 v[40:41], v[58:59], v[62:63], v[40:41] op_sel_hi:[0,1,1]
	v_cvt_f32_i32_sdwa v53, sext(v53) dst_sel:DWORD dst_unused:UNUSED_PAD src0_sel:WORD_0
	v_cvt_f32_i32_sdwa v52, sext(v52) dst_sel:DWORD dst_unused:UNUSED_PAD src0_sel:WORD_0
	v_cvt_f32_i32_sdwa v63, sext(v8) dst_sel:DWORD dst_unused:UNUSED_PAD src0_sel:WORD_1
	v_cvt_f32_i32_sdwa v62, sext(v5) dst_sel:DWORD dst_unused:UNUSED_PAD src0_sel:WORD_1
	v_cvt_f32_i32_sdwa v55, sext(v55) dst_sel:DWORD dst_unused:UNUSED_PAD src0_sel:WORD_0
	v_cvt_f32_i32_sdwa v54, sext(v54) dst_sel:DWORD dst_unused:UNUSED_PAD src0_sel:WORD_0
	v_add_u32_e32 v50, s14, v50
	v_pk_fma_f32 v[18:19], v[58:59], v[56:57], v[18:19] op_sel_hi:[0,1,1]
	v_pk_mul_f32 v[56:57], v[58:59], v[52:53] op_sel_hi:[0,1]
	v_pk_fma_f32 v[32:33], v[58:59], v[52:53], v[32:33] op_sel_hi:[0,1,1]
	v_pk_mul_f32 v[52:53], v[58:59], v[62:63] op_sel_hi:[0,1]
	v_ashrrev_i32_e32 v51, 31, v50
	v_cvt_pk_f16_f32 v5, v52, v53
	v_pk_fma_f32 v[10:11], v[52:53], v[52:53], v[10:11]
	v_pk_mul_f32 v[52:53], v[58:59], v[54:55] op_sel_hi:[0,1]
	v_lshlrev_b64 v[50:51], 8, v[50:51]
	v_cvt_pk_f16_f32 v9, v52, v53
	v_pk_fma_f32 v[24:25], v[52:53], v[52:53], v[24:25]
	v_lshl_add_u64 v[50:51], s[8:9], 0, v[50:51]
	v_lshlrev_b32_e32 v52, 1, v42
	v_mov_b32_e32 v53, 0
	v_cvt_pk_f16_f32 v8, v56, v57
	v_pk_fma_f32 v[30:31], v[56:57], v[56:57], v[30:31]
	v_pk_fma_f32 v[12:13], v[58:59], v[62:63], v[12:13] op_sel_hi:[0,1,1]
	v_pk_fma_f32 v[26:27], v[58:59], v[54:55], v[26:27] op_sel_hi:[0,1,1]
	v_lshl_add_u64 v[50:51], v[50:51], 0, v[52:53]
	global_store_dwordx4 v[50:51], v[6:9], off sc1
	global_store_dwordx4 v[50:51], v[2:5], off offset:128 sc1
.LBB2_20:
	s_or_b64 exec, exec, s[4:5]
	s_and_saveexec_b64 s[4:5], vcc
	s_cbranch_execz .LBB2_28
	v_or_b32_e32 v50, 0x100, v43
	v_cmp_gt_u32_e32 vcc, s15, v50
	s_and_saveexec_b64 s[6:7], vcc
	s_cbranch_execz .LBB2_23
	s_movk_i32 s12, 0x140
	v_mad_u32_u24 v6, v50, s12, v47
	s_waitcnt vmcnt(4)
	ds_read_b128 v[2:5], v6
	ds_read_b128 v[52:55], v6 offset:16
	s_mov_b32 s12, 0xb4c00000
	s_waitcnt vmcnt(3)
	v_mul_lo_u32 v49, v49, s12
	s_waitcnt vmcnt(2)
	v_mul_f32_e32 v48, v48, v45
	s_waitcnt lgkmcnt(1)
	v_add_u32_e32 v6, v2, v49
	v_add_u32_e32 v7, v3, v49
	v_sub_u32_sdwa v7, v7, sext(v3) dst_sel:DWORD dst_unused:UNUSED_PAD src0_sel:DWORD src1_sel:WORD_0
	v_sub_u32_sdwa v6, v6, sext(v2) dst_sel:DWORD dst_unused:UNUSED_PAD src0_sel:DWORD src1_sel:WORD_0
	v_cvt_f32_i32_sdwa v7, sext(v7) dst_sel:DWORD dst_unused:UNUSED_PAD src0_sel:WORD_1
	v_cvt_f32_i32_sdwa v6, sext(v6) dst_sel:DWORD dst_unused:UNUSED_PAD src0_sel:WORD_1
	v_cvt_f32_i32_sdwa v57, sext(v3) dst_sel:DWORD dst_unused:UNUSED_PAD src0_sel:WORD_0
	v_cvt_f32_i32_sdwa v56, sext(v2) dst_sel:DWORD dst_unused:UNUSED_PAD src0_sel:WORD_0
	v_add_u32_e32 v3, v4, v49
	v_pk_mul_f32 v[8:9], v[48:49], v[6:7] op_sel_hi:[0,1]
	v_pk_fma_f32 v[28:29], v[48:49], v[6:7], v[28:29] op_sel_hi:[0,1,1]
	v_add_u32_e32 v6, v5, v49
	v_sub_u32_sdwa v6, v6, sext(v5) dst_sel:DWORD dst_unused:UNUSED_PAD src0_sel:DWORD src1_sel:WORD_0
	v_sub_u32_sdwa v3, v3, sext(v4) dst_sel:DWORD dst_unused:UNUSED_PAD src0_sel:DWORD src1_sel:WORD_0
	v_cvt_f32_i32_sdwa v59, sext(v6) dst_sel:DWORD dst_unused:UNUSED_PAD src0_sel:WORD_1
	v_cvt_f32_i32_sdwa v58, sext(v3) dst_sel:DWORD dst_unused:UNUSED_PAD src0_sel:WORD_1
	s_waitcnt lgkmcnt(0)
	v_add_u32_e32 v7, v52, v49
	v_add_u32_e32 v51, v53, v49
	v_cvt_f32_i32_sdwa v5, sext(v5) dst_sel:DWORD dst_unused:UNUSED_PAD src0_sel:WORD_0
	v_cvt_f32_i32_sdwa v4, sext(v4) dst_sel:DWORD dst_unused:UNUSED_PAD src0_sel:WORD_0
	v_sub_u32_sdwa v51, v51, sext(v53) dst_sel:DWORD dst_unused:UNUSED_PAD src0_sel:DWORD src1_sel:WORD_0
	v_sub_u32_sdwa v7, v7, sext(v52) dst_sel:DWORD dst_unused:UNUSED_PAD src0_sel:DWORD src1_sel:WORD_0
	v_cvt_pk_f16_f32 v2, v8, v9
	v_pk_fma_f32 v[20:21], v[8:9], v[8:9], v[20:21]
	v_pk_mul_f32 v[8:9], v[48:49], v[56:57] op_sel_hi:[0,1]
	v_pk_fma_f32 v[40:41], v[48:49], v[56:57], v[40:41] op_sel_hi:[0,1,1]
	v_cvt_f32_i32_sdwa v57, sext(v51) dst_sel:DWORD dst_unused:UNUSED_PAD src0_sel:WORD_1
	v_cvt_f32_i32_sdwa v56, sext(v7) dst_sel:DWORD dst_unused:UNUSED_PAD src0_sel:WORD_1
	v_cvt_pk_f16_f32 v6, v8, v9
	v_pk_fma_f32 v[38:39], v[8:9], v[8:9], v[38:39]
	v_pk_mul_f32 v[8:9], v[48:49], v[58:59] op_sel_hi:[0,1]
	v_cvt_pk_f16_f32 v3, v8, v9
	v_pk_fma_f32 v[16:17], v[8:9], v[8:9], v[16:17]
	v_pk_mul_f32 v[8:9], v[48:49], v[4:5] op_sel_hi:[0,1]
	v_cvt_pk_f16_f32 v7, v8, v9
	v_pk_fma_f32 v[34:35], v[8:9], v[8:9], v[34:35]
	v_pk_mul_f32 v[8:9], v[48:49], v[56:57] op_sel_hi:[0,1]
	v_pk_fma_f32 v[36:37], v[48:49], v[4:5], v[36:37] op_sel_hi:[0,1,1]
	v_cvt_pk_f16_f32 v4, v8, v9
	v_pk_fma_f32 v[14:15], v[8:9], v[8:9], v[14:15]
	v_add_u32_e32 v5, v54, v49
	v_add_u32_e32 v8, v55, v49
	v_sub_u32_sdwa v8, v8, sext(v55) dst_sel:DWORD dst_unused:UNUSED_PAD src0_sel:DWORD src1_sel:WORD_0
	v_sub_u32_sdwa v5, v5, sext(v54) dst_sel:DWORD dst_unused:UNUSED_PAD src0_sel:DWORD src1_sel:WORD_0
	v_pk_fma_f32 v[22:23], v[48:49], v[58:59], v[22:23] op_sel_hi:[0,1,1]
	v_cvt_f32_i32_sdwa v53, sext(v53) dst_sel:DWORD dst_unused:UNUSED_PAD src0_sel:WORD_0
	v_cvt_f32_i32_sdwa v52, sext(v52) dst_sel:DWORD dst_unused:UNUSED_PAD src0_sel:WORD_0
	v_cvt_f32_i32_sdwa v59, sext(v8) dst_sel:DWORD dst_unused:UNUSED_PAD src0_sel:WORD_1
	v_cvt_f32_i32_sdwa v58, sext(v5) dst_sel:DWORD dst_unused:UNUSED_PAD src0_sel:WORD_1
	v_cvt_f32_i32_sdwa v55, sext(v55) dst_sel:DWORD dst_unused:UNUSED_PAD src0_sel:WORD_0
	v_cvt_f32_i32_sdwa v54, sext(v54) dst_sel:DWORD dst_unused:UNUSED_PAD src0_sel:WORD_0
	v_pk_fma_f32 v[18:19], v[48:49], v[56:57], v[18:19] op_sel_hi:[0,1,1]
	v_pk_mul_f32 v[56:57], v[48:49], v[52:53] op_sel_hi:[0,1]
	v_pk_fma_f32 v[32:33], v[48:49], v[52:53], v[32:33] op_sel_hi:[0,1,1]
	v_pk_mul_f32 v[52:53], v[48:49], v[58:59] op_sel_hi:[0,1]
	v_cvt_pk_f16_f32 v5, v52, v53
	v_pk_fma_f32 v[12:13], v[48:49], v[58:59], v[12:13] op_sel_hi:[0,1,1]
	v_pk_fma_f32 v[10:11], v[52:53], v[52:53], v[10:11]
	v_pk_mul_f32 v[52:53], v[48:49], v[54:55] op_sel_hi:[0,1]
	v_pk_fma_f32 v[26:27], v[48:49], v[54:55], v[26:27] op_sel_hi:[0,1,1]
	v_add_u32_e32 v48, s14, v50
	v_ashrrev_i32_e32 v49, 31, v48
	v_lshlrev_b64 v[48:49], 8, v[48:49]
	v_lshl_add_u64 v[48:49], s[8:9], 0, v[48:49]
	v_lshlrev_b32_e32 v50, 1, v42
	v_mov_b32_e32 v51, 0
	v_cvt_pk_f16_f32 v8, v56, v57
	v_pk_fma_f32 v[30:31], v[56:57], v[56:57], v[30:31]
	v_cvt_pk_f16_f32 v9, v52, v53
	v_pk_fma_f32 v[24:25], v[52:53], v[52:53], v[24:25]
	v_lshl_add_u64 v[48:49], v[48:49], 0, v[50:51]
	global_store_dwordx4 v[48:49], v[6:9], off sc1
	global_store_dwordx4 v[48:49], v[2:5], off offset:128 sc1
.LBB2_23:
	s_or_b64 exec, exec, s[6:7]
	s_and_saveexec_b64 s[6:7], vcc
	s_cbranch_execz .LBB2_27
	v_or_b32_e32 v43, 0x180, v43
	v_cmp_gt_u32_e32 vcc, s15, v43
	s_and_saveexec_b64 s[12:13], vcc
	s_cbranch_execz .LBB2_26
	s_movk_i32 s15, 0x140
	v_mad_u32_u24 v6, v43, s15, v47
	s_waitcnt vmcnt(4)
	ds_read_b128 v[2:5], v6
	s_mov_b32 s15, 0xb4c00000
	s_waitcnt vmcnt(0)
	v_mul_lo_u32 v54, v46, s15
	ds_read_b128 v[46:49], v6 offset:16
	v_mul_f32_e32 v44, v44, v45
	s_waitcnt lgkmcnt(1)
	v_add_u32_e32 v6, v2, v54
	v_add_u32_e32 v7, v3, v54
	v_sub_u32_sdwa v7, v7, sext(v3) dst_sel:DWORD dst_unused:UNUSED_PAD src0_sel:DWORD src1_sel:WORD_0
	v_sub_u32_sdwa v6, v6, sext(v2) dst_sel:DWORD dst_unused:UNUSED_PAD src0_sel:DWORD src1_sel:WORD_0
	v_cvt_f32_i32_sdwa v7, sext(v7) dst_sel:DWORD dst_unused:UNUSED_PAD src0_sel:WORD_1
	v_cvt_f32_i32_sdwa v6, sext(v6) dst_sel:DWORD dst_unused:UNUSED_PAD src0_sel:WORD_1
	v_cvt_f32_i32_sdwa v51, sext(v3) dst_sel:DWORD dst_unused:UNUSED_PAD src0_sel:WORD_0
	v_add_u32_e32 v3, v4, v54
	v_cvt_f32_i32_sdwa v50, sext(v2) dst_sel:DWORD dst_unused:UNUSED_PAD src0_sel:WORD_0
	v_pk_mul_f32 v[8:9], v[44:45], v[6:7] op_sel_hi:[0,1]
	v_pk_fma_f32 v[28:29], v[44:45], v[6:7], v[28:29] op_sel_hi:[0,1,1]
	v_add_u32_e32 v6, v5, v54
	v_sub_u32_sdwa v6, v6, sext(v5) dst_sel:DWORD dst_unused:UNUSED_PAD src0_sel:DWORD src1_sel:WORD_0
	v_sub_u32_sdwa v3, v3, sext(v4) dst_sel:DWORD dst_unused:UNUSED_PAD src0_sel:DWORD src1_sel:WORD_0
	v_cvt_f32_i32_sdwa v53, sext(v6) dst_sel:DWORD dst_unused:UNUSED_PAD src0_sel:WORD_1
	v_cvt_f32_i32_sdwa v52, sext(v3) dst_sel:DWORD dst_unused:UNUSED_PAD src0_sel:WORD_1
	v_cvt_f32_i32_sdwa v5, sext(v5) dst_sel:DWORD dst_unused:UNUSED_PAD src0_sel:WORD_0
	v_cvt_f32_i32_sdwa v4, sext(v4) dst_sel:DWORD dst_unused:UNUSED_PAD src0_sel:WORD_0
	v_cvt_pk_f16_f32 v2, v8, v9
	v_pk_fma_f32 v[20:21], v[8:9], v[8:9], v[20:21]
	v_pk_mul_f32 v[8:9], v[44:45], v[50:51] op_sel_hi:[0,1]
	v_cvt_pk_f16_f32 v6, v8, v9
	v_pk_fma_f32 v[38:39], v[8:9], v[8:9], v[38:39]
	v_pk_mul_f32 v[8:9], v[44:45], v[52:53] op_sel_hi:[0,1]
	v_pk_fma_f32 v[40:41], v[44:45], v[50:51], v[40:41] op_sel_hi:[0,1,1]
	v_cvt_pk_f16_f32 v3, v8, v9
	v_pk_fma_f32 v[22:23], v[44:45], v[52:53], v[22:23] op_sel_hi:[0,1,1]
	v_pk_fma_f32 v[16:17], v[8:9], v[8:9], v[16:17]
	v_pk_mul_f32 v[8:9], v[44:45], v[4:5] op_sel_hi:[0,1]
	s_waitcnt lgkmcnt(0)
	v_add_u32_e32 v7, v46, v54
	v_add_u32_e32 v45, v47, v54
	v_sub_u32_sdwa v45, v45, sext(v47) dst_sel:DWORD dst_unused:UNUSED_PAD src0_sel:DWORD src1_sel:WORD_0
	v_sub_u32_sdwa v7, v7, sext(v46) dst_sel:DWORD dst_unused:UNUSED_PAD src0_sel:DWORD src1_sel:WORD_0
	v_cvt_f32_i32_sdwa v51, sext(v45) dst_sel:DWORD dst_unused:UNUSED_PAD src0_sel:WORD_1
	v_cvt_f32_i32_sdwa v50, sext(v7) dst_sel:DWORD dst_unused:UNUSED_PAD src0_sel:WORD_1
	v_cvt_pk_f16_f32 v7, v8, v9
	v_pk_fma_f32 v[34:35], v[8:9], v[8:9], v[34:35]
	v_pk_fma_f32 v[36:37], v[44:45], v[4:5], v[36:37] op_sel_hi:[0,1,1]
	v_pk_mul_f32 v[8:9], v[44:45], v[50:51] op_sel_hi:[0,1]
	v_cvt_pk_f16_f32 v4, v8, v9
	v_pk_fma_f32 v[14:15], v[8:9], v[8:9], v[14:15]
	v_add_u32_e32 v5, v48, v54
	v_add_u32_e32 v8, v49, v54
	v_sub_u32_sdwa v8, v8, sext(v49) dst_sel:DWORD dst_unused:UNUSED_PAD src0_sel:DWORD src1_sel:WORD_0
	v_sub_u32_sdwa v5, v5, sext(v48) dst_sel:DWORD dst_unused:UNUSED_PAD src0_sel:DWORD src1_sel:WORD_0
	v_cvt_f32_i32_sdwa v47, sext(v47) dst_sel:DWORD dst_unused:UNUSED_PAD src0_sel:WORD_0
	v_cvt_f32_i32_sdwa v46, sext(v46) dst_sel:DWORD dst_unused:UNUSED_PAD src0_sel:WORD_0
	v_cvt_f32_i32_sdwa v53, sext(v8) dst_sel:DWORD dst_unused:UNUSED_PAD src0_sel:WORD_1
	v_cvt_f32_i32_sdwa v52, sext(v5) dst_sel:DWORD dst_unused:UNUSED_PAD src0_sel:WORD_1
	v_cvt_f32_i32_sdwa v49, sext(v49) dst_sel:DWORD dst_unused:UNUSED_PAD src0_sel:WORD_0
	v_cvt_f32_i32_sdwa v48, sext(v48) dst_sel:DWORD dst_unused:UNUSED_PAD src0_sel:WORD_0
	v_pk_fma_f32 v[18:19], v[44:45], v[50:51], v[18:19] op_sel_hi:[0,1,1]
	v_pk_mul_f32 v[50:51], v[44:45], v[46:47] op_sel_hi:[0,1]
	v_pk_fma_f32 v[32:33], v[44:45], v[46:47], v[32:33] op_sel_hi:[0,1,1]
	v_pk_mul_f32 v[46:47], v[44:45], v[52:53] op_sel_hi:[0,1]
	v_cvt_pk_f16_f32 v5, v46, v47
	v_pk_fma_f32 v[12:13], v[44:45], v[52:53], v[12:13] op_sel_hi:[0,1,1]
	v_pk_fma_f32 v[10:11], v[46:47], v[46:47], v[10:11]
	v_pk_mul_f32 v[46:47], v[44:45], v[48:49] op_sel_hi:[0,1]
	v_pk_fma_f32 v[26:27], v[44:45], v[48:49], v[26:27] op_sel_hi:[0,1,1]
	v_add_u32_e32 v44, s14, v43
	v_ashrrev_i32_e32 v45, 31, v44
	v_lshlrev_b64 v[44:45], 8, v[44:45]
	v_lshl_add_u64 v[44:45], s[8:9], 0, v[44:45]
	v_lshlrev_b32_e32 v42, 1, v42
	v_mov_b32_e32 v43, 0
	v_cvt_pk_f16_f32 v8, v50, v51
	v_pk_fma_f32 v[30:31], v[50:51], v[50:51], v[30:31]
	v_cvt_pk_f16_f32 v9, v46, v47
	v_pk_fma_f32 v[24:25], v[46:47], v[46:47], v[24:25]
	v_lshl_add_u64 v[42:43], v[44:45], 0, v[42:43]
	global_store_dwordx4 v[42:43], v[6:9], off sc1
	global_store_dwordx4 v[42:43], v[2:5], off offset:128 sc1
